# speedup vs baseline: 1.0026x; 1.0026x over previous
.LBB1_4:
	s_or_b64 exec, exec, s[22:23]
	s_load_dwordx4 s[68:71], s[0:1], 0x8
	s_load_dwordx2 s[4:5], s[0:1], 0x18
	s_and_b32 s22, s2, 7
	s_bfe_u32 s66, s3, 0x20006
	s_lshr_b32 s67, s3, 8
	s_mul_i32 s33, s22, 0x30000
	s_waitcnt lgkmcnt(0)
	s_add_u32 s22, s4, s33
	s_addc_u32 s23, s5, 0
	s_add_u32 s4, s68, s33
	s_addc_u32 s5, s69, 0
	s_add_u32 s34, s70, s33
	s_addc_u32 s35, s71, 0
	s_lshl_b32 s68, s66, 6
	s_mul_i32 s69, s67, 0x900
	v_and_b32_e32 v100, 63, v0
	s_or_b32 s64, s68, s69
	v_or_b32_e32 v2, s64, v100
	s_add_i32 s65, s64, 0x100
	v_ashrrev_i32_e32 v3, 31, v2
	v_or_b32_e32 v4, s65, v100
	v_lshl_add_u64 v[2:3], v[2:3], 4, s[22:23]
	v_ashrrev_i32_e32 v5, 31, v4
	s_add_i32 s65, s64, 0x200
	v_lshl_add_u64 v[4:5], v[4:5], 4, s[22:23]
	global_load_dwordx4 v[82:85], v[2:3], off
	global_load_dwordx4 v[74:77], v[4:5], off
	v_or_b32_e32 v2, s65, v100
	s_add_i32 s65, s64, 0x300
	v_ashrrev_i32_e32 v3, 31, v2
	v_or_b32_e32 v4, s65, v100
	v_lshl_add_u64 v[2:3], v[2:3], 4, s[22:23]
	v_ashrrev_i32_e32 v5, 31, v4
	s_addk_i32 s64, 0x400
	v_lshl_add_u64 v[4:5], v[4:5], 4, s[22:23]
	global_load_dwordx4 v[78:81], v[2:3], off
	global_load_dwordx4 v[70:73], v[4:5], off
	v_or_b32_e32 v2, s64, v100
	v_ashrrev_i32_e32 v3, 31, v2
	v_lshl_add_u64 v[2:3], v[2:3], 4, s[22:23]
	v_mov_b32_e32 v99, 0
	v_lshlrev_b32_e32 v98, 4, v100
	global_load_dwordx4 v[66:69], v[2:3], off
	s_add_i32 s65, s64, 0x100
	v_or_b32_e32 v2, s65, v100
	v_mov_b32_e32 v3, 0
	v_lshl_add_u64 v[2:3], v[2:3], 4, s[22:23]
	global_load_dwordx4 v[108:111], v[2:3], off
	s_add_i32 s65, s64, 0x200
	v_or_b32_e32 v2, s65, v100
	v_mov_b32_e32 v3, 0
	v_lshl_add_u64 v[2:3], v[2:3], 4, s[22:23]
	global_load_dwordx4 v[118:121], v[2:3], off
	s_add_i32 s65, s64, 0x300
	v_or_b32_e32 v2, s65, v100
	v_mov_b32_e32 v3, 0
	v_lshl_add_u64 v[2:3], v[2:3], 4, s[22:23]
	global_load_dwordx4 v[122:125], v[2:3], off
	v_lshl_add_u64 v[2:3], s[4:5], 0, v[98:99]
	v_bfe_u32 v115, v0, 5, 1
	v_add_co_u32_e32 v2, vcc, 0x1000, v2
	v_lshlrev_b32_e32 v1, 2, v115
	s_nop 0
	v_addc_co_u32_e32 v3, vcc, 0, v3, vcc
	global_load_dwordx4 v[86:89], v98, s[4:5]
	global_load_dwordx4 v[62:65], v98, s[4:5] offset:1024
	global_load_dwordx4 v[58:61], v98, s[4:5] offset:2048
	global_load_dwordx4 v[54:57], v98, s[4:5] offset:3072
	global_load_dwordx4 v[50:53], v[2:3], off
	s_nop 0
	global_load_dword v2, v1, s[34:35]
	global_load_dword v6, v1, s[34:35] offset:8
	global_load_dword v10, v1, s[34:35] offset:16
	global_load_dword v14, v1, s[34:35] offset:24
	s_cmp_gt_u32 s3, 63
	s_cselect_b64 s[34:35], -1, 0
	s_and_b64 vcc, exec, s[34:35]
	s_cbranch_vccz .LBB1_46
	v_cmp_gt_u32_e64 s[4:5], 21, v0
	v_lshlrev_b32_e32 v1, 2, v0
	s_and_saveexec_b64 s[64:65], s[4:5]
	s_cbranch_execnz .LBB1_47

.LBB1_15:
	s_or_b64 exec, exec, s[12:13]
	v_and_b32_e32 v114, 31, v0
	s_mul_i32 s9, s67, 0x60
	v_or_b32_e32 v15, s9, v114
	v_min_u32_e32 v91, 0xa8, v15
	v_mul_lo_u16_e32 v15, 0x4f, v91
	s_lshl_b32 s7, s66, 3
	v_lshrrev_b16_e32 v15, 9, v15
	s_or_b32 s8, s7, 0xb600
	v_and_b32_e32 v15, 62, v15
	v_add_u32_e32 v15, v91, v15
	s_movk_i32 s6, 0x48
	v_mov_b32_e32 v99, s8
	v_mad_u32_u24 v42, v15, s6, v99
	v_mad_u32_u24 v43, v115, s6, v42
	s_waitcnt lgkmcnt(0)
	s_barrier
	ds_read2_b64 v[34:37], v43 offset1:1
	ds_read2_b64 v[38:41], v43 offset0:135 offset1:136
	s_waitcnt vmcnt(3)
	v_mov_b32_e32 v3, v2
	v_mov_b32_e32 v4, v2
	v_mov_b32_e32 v5, v2
	s_waitcnt vmcnt(2)
	v_mov_b32_e32 v7, v6
	v_mov_b32_e32 v8, v6
	v_mov_b32_e32 v9, v6
	s_waitcnt vmcnt(1)
	v_mov_b32_e32 v11, v10
	v_mov_b32_e32 v12, v10
	v_mov_b32_e32 v13, v10
	s_waitcnt vmcnt(0)
	v_mov_b32_e32 v15, v14
	v_mov_b32_e32 v16, v14
	v_mov_b32_e32 v17, v14
	s_movk_i32 s8, 0x438
	s_add_i32 s12, s9, 32
	s_waitcnt lgkmcnt(1)
	v_mfma_f32_32x32x16_f16 v[18:33], v[86:89], v[34:37], v[2:17]
	v_add_u32_e32 v34, 0x8b8, v43
	ds_read2_b64 v[34:37], v34 offset1:1
	v_and_or_b32 v107, v0, 32, s7
	s_movk_i32 s7, 0x110
	v_mad_u32_u24 v91, v91, s7, v107
	s_add_i32 s9, s9, 64
	s_lshr_b32 s42, s3, 6
	s_waitcnt lgkmcnt(1)
	v_mfma_f32_32x32x16_f16 v[18:33], v[62:65], v[38:41], v[18:33]
	v_mad_u32_u24 v38, v115, s8, v42
	ds_read2_b64 v[38:41], v38 offset0:18 offset1:19
	s_cmpk_lt_u32 s3, 0x100
	s_cselect_b64 s[30:31], -1, 0
	s_add_i32 s13, s69, 0x600
	s_add_i32 s14, s69, 0x700
	v_lshlrev_b32_e32 v116, 4, v115
	s_waitcnt lgkmcnt(1)
	v_mfma_f32_32x32x16_f16 v[18:33], v[58:61], v[34:37], v[18:33]
	v_add_u32_e32 v34, 0x870, v43
	ds_read2_b64 v[34:37], v34 offset1:1
	s_movk_i32 s15, 0x1070
	s_movk_i32 s16, 0x1ba0
	s_movk_i32 s17, 0x1c20
	s_waitcnt lgkmcnt(1)
	v_mfma_f32_32x32x16_f16 v[18:33], v[54:57], v[38:41], v[18:33]
	v_or_b32_e32 v38, s12, v114
	v_min_u32_e32 v101, 0xa8, v38
	v_mul_lo_u16_e32 v38, 0x4f, v101
	v_lshrrev_b16_e32 v38, 9, v38
	v_and_b32_e32 v38, 62, v38
	v_add_u32_e32 v38, v101, v38
	v_mad_u32_u24 v97, v38, s6, v99
	v_mad_u32_u24 v106, v115, s6, v97
	ds_read2_b64 v[92:95], v106 offset1:1
	v_add_u32_e32 v96, 0x8b8, v106
	ds_read2_b64 v[102:105], v96 offset1:1
	s_waitcnt lgkmcnt(2)
	v_mfma_f32_32x32x16_f16 v[18:33], v[50:53], v[34:37], v[18:33]
	s_add_i32 s12, s69, 0x500
	s_addk_i32 s69, 0x800
	s_cmpk_gt_u32 s3, 0xff
	s_cselect_b64 vcc, -1, 0
	s_waitcnt lgkmcnt(1)
	v_mfma_f32_32x32x16_f16 v[34:49], v[86:89], v[92:95], v[2:17]
	ds_read2_b64 v[92:95], v106 offset0:135 offset1:136
	s_nop 4
	v_cvt_pk_f16_f32 v18, v18, v19
	v_pk_max_f16 v96, v18, 0
	v_mad_u32_u24 v18, v115, s8, v97
	v_cvt_pk_f16_f32 v22, v22, v23
	v_add_u32_e32 v23, 0x870, v106
	v_cvt_pk_f16_f32 v30, v30, v31
	s_waitcnt lgkmcnt(0)
	v_mfma_f32_32x32x16_f16 v[34:49], v[62:65], v[92:95], v[34:49]
	v_cvt_pk_f16_f32 v92, v20, v21
	ds_read2_b64 v[18:21], v18 offset0:18 offset1:19
	v_pk_max_f16 v97, v92, 0
	ds_read2_b64 v[92:95], v23 offset1:1
	v_cvt_pk_f16_f32 v31, v32, v33
	v_mfma_f32_32x32x16_f16 v[34:49], v[58:61], v[102:105], v[34:49]
	v_or_b32_e32 v102, 64, v114
	s_waitcnt lgkmcnt(1)
	v_mfma_f32_32x32x16_f16 v[34:49], v[54:57], v[18:21], v[34:49]
	v_cvt_pk_f16_f32 v19, v24, v25
	v_pk_max_f16 v18, v22, 0
	v_pk_max_f16 v19, v19, 0
	ds_write2_b64 v91, v[96:97], v[18:19] offset1:8
	v_cvt_pk_f16_f32 v18, v26, v27
	v_pk_max_f16 v26, v18, 0
	v_or_b32_e32 v18, s9, v114
	v_cvt_pk_f16_f32 v22, v28, v29
	v_min_u32_e32 v28, 0xa8, v18
	v_mul_lo_u16_e32 v18, 0x4f, v28
	v_lshrrev_b16_e32 v18, 9, v18
	v_and_b32_e32 v18, 62, v18
	v_add_u32_e32 v18, v28, v18
	v_mad_u32_u24 v29, v18, s6, v99
	s_waitcnt lgkmcnt(1)
	v_mfma_f32_32x32x16_f16 v[34:49], v[50:53], v[92:95], v[34:49]
	v_add_u32_e32 v94, s68, v100
	v_add_u32_e32 v94, s69, v94
	v_mov_b32_e32 v95, 0
	v_lshl_add_u64 v[94:95], v[94:95], 4, s[22:23]
	global_load_dwordx4 v[94:97], v[94:95], off
	v_mad_u32_u24 v92, v115, s6, v29
	ds_read2_b64 v[18:21], v92 offset1:1
	v_pk_max_f16 v27, v22, 0
	ds_read2_b64 v[22:25], v92 offset0:135 offset1:136
	v_or_b32_e32 v99, 32, v114
	s_nop 6
	v_cvt_pk_f16_f32 v32, v40, v41
	s_waitcnt lgkmcnt(1)
	v_mfma_f32_32x32x16_f16 v[2:17], v[86:89], v[18:21], v[2:17]
	v_pk_max_f16 v18, v30, 0
	v_pk_max_f16 v19, v31, 0
	ds_write2_b64 v91, v[26:27], v[18:19] offset0:16 offset1:24
	v_cvt_pk_f16_f32 v18, v34, v35
	v_cvt_pk_f16_f32 v19, v36, v37
	v_pk_max_f16 v26, v18, 0
	v_add_u32_e32 v18, 0x8b8, v92
	s_waitcnt lgkmcnt(1)
	v_mfma_f32_32x32x16_f16 v[2:17], v[62:65], v[22:25], v[2:17]
	v_pk_max_f16 v27, v19, 0
	ds_read2_b64 v[18:21], v18 offset1:1
	v_mad_u32_u24 v22, v115, s8, v29
	ds_read2_b64 v[22:25], v22 offset0:18 offset1:19
	v_cvt_pk_f16_f32 v31, v38, v39
	v_mad_u32_u24 v30, v101, s7, v107
	s_and_b64 s[8:9], vcc, exec
	s_waitcnt lgkmcnt(1)
	v_mfma_f32_32x32x16_f16 v[2:17], v[58:61], v[18:21], v[2:17]
	v_pk_max_f16 v18, v31, 0
	v_pk_max_f16 v19, v32, 0
	ds_write2_b64 v30, v[26:27], v[18:19] offset1:8
	v_cvt_pk_f16_f32 v18, v42, v43
	v_cvt_pk_f16_f32 v19, v44, v45
	v_pk_max_f16 v26, v18, 0
	v_add_u32_e32 v18, 0x870, v92
	s_waitcnt lgkmcnt(1)
	v_mfma_f32_32x32x16_f16 v[2:17], v[54:57], v[22:25], v[2:17]
	v_pk_max_f16 v27, v19, 0
	ds_read2_b64 v[18:21], v18 offset1:1
	v_cvt_pk_f16_f32 v22, v46, v47
	v_cvt_pk_f16_f32 v23, v48, v49
	v_pk_max_f16 v22, v22, 0
	v_pk_max_f16 v23, v23, 0
	ds_write2_b64 v30, v[26:27], v[22:23] offset0:16 offset1:24
	s_waitcnt lgkmcnt(1)
	v_mfma_f32_32x32x16_f16 v[2:17], v[50:53], v[18:21], v[2:17]
	v_mad_u32_u24 v18, v28, s7, v107
	v_lshl_or_b32 v42, s66, 5, v116
	s_cselect_b32 s8, 0xf60, 0
	s_movk_i32 s9, 0xff0
	s_cselect_b32 s9, s9, 0x80
	s_cselect_b32 s15, s15, 0x110
	s_cselect_b32 s16, s16, 0x190
	s_nop 4
	v_cvt_pk_f16_f32 v2, v2, v3
	v_cvt_pk_f16_f32 v3, v4, v5
	v_cvt_pk_f16_f32 v4, v6, v7
	v_cvt_pk_f16_f32 v5, v8, v9
	v_pk_max_f16 v2, v2, 0
	v_pk_max_f16 v3, v3, 0
	v_pk_max_f16 v4, v4, 0
	v_pk_max_f16 v5, v5, 0
	ds_write2_b64 v18, v[2:3], v[4:5] offset1:8
	v_cvt_pk_f16_f32 v2, v10, v11
	v_cvt_pk_f16_f32 v3, v12, v13
	v_cvt_pk_f16_f32 v4, v14, v15
	v_cvt_pk_f16_f32 v5, v16, v17
	v_pk_max_f16 v2, v2, 0
	v_pk_max_f16 v3, v3, 0
	v_pk_max_f16 v4, v4, 0
	v_pk_max_f16 v5, v5, 0
	ds_write2_b64 v18, v[2:3], v[4:5] offset0:16 offset1:24
	v_mul_lo_u16_e32 v2, 24, v114
	v_lshrrev_b16_e32 v2, 7, v2
	v_and_b32_e32 v2, 6, v2
	v_add_u32_sdwa v103, v114, v2 dst_sel:DWORD dst_unused:UNUSED_PAD src0_sel:DWORD src1_sel:WORD_0
	v_mul_lo_u16_e32 v2, 47, v99
	v_mov_b32_e32 v3, 14
	v_and_b32_sdwa v6, v2, v3 dst_sel:DWORD dst_unused:UNUSED_PAD src0_sel:BYTE_1 src1_sel:DWORD
	v_add_u32_e32 v106, v99, v6
	v_mad_u32_u24 v90, v103, s7, v42
	v_mad_u32_u24 v91, v106, s7, v42
	v_add_u32_e32 v2, s8, v90
	v_add_u32_e32 v6, s8, v91
	s_waitcnt lgkmcnt(0)
	s_barrier
	ds_read_b128 v[2:5], v2
	ds_read_b128 v[6:9], v6
	s_waitcnt lgkmcnt(1)
	v_mfma_f32_32x32x16_f16 v[18:33], v[82:85], v[2:5], 0
	v_add_u32_e32 v34, s9, v90
	v_add_u32_e32 v38, s9, v91
	ds_read_b128 v[34:37], v34
	ds_read_b128 v[38:41], v38
	s_cselect_b32 s17, s17, 0x220
	v_or_b32_e32 v101, 0x60, v114
	s_waitcnt lgkmcnt(2)
	v_mfma_f32_32x32x16_f16 v[2:17], v[82:85], v[6:9], 0
	s_waitcnt lgkmcnt(1)
	v_mfma_f32_32x32x16_f16 v[18:33], v[74:77], v[34:37], v[18:33]
	v_add_u32_e32 v34, s15, v90
	ds_read_b128 v[34:37], v34
	s_waitcnt lgkmcnt(1)
	v_mfma_f32_32x32x16_f16 v[2:17], v[74:77], v[38:41], v[2:17]
	v_add_u32_e32 v38, s15, v91
	ds_read_b128 v[38:41], v38
	s_waitcnt lgkmcnt(1)
	v_mfma_f32_32x32x16_f16 v[18:33], v[78:81], v[34:37], v[18:33]
	v_add_u32_e32 v34, s16, v90
	ds_read_b128 v[34:37], v34
	s_waitcnt lgkmcnt(1)
	v_mfma_f32_32x32x16_f16 v[2:17], v[78:81], v[38:41], v[2:17]
	v_add_u32_e32 v38, s16, v91
	ds_read_b128 v[38:41], v38
	s_waitcnt lgkmcnt(1)
	v_mfma_f32_32x32x16_f16 v[18:33], v[70:73], v[34:37], v[18:33]
	v_mul_lo_u16_e32 v34, 0xbb, v102
	v_lshrrev_b16_e32 v34, 10, v34
	v_and_b32_e32 v43, 30, v34
	v_add_u32_e32 v34, s17, v90
	ds_read_b128 v[34:37], v34
	v_add_u32_e32 v104, v102, v43
	v_mad_u32_u24 v92, v104, s7, v42
	s_waitcnt lgkmcnt(1)
	v_mfma_f32_32x32x16_f16 v[2:17], v[70:73], v[38:41], v[2:17]
	v_add_u32_e32 v38, s17, v91
	ds_read_b128 v[38:41], v38
	s_waitcnt lgkmcnt(1)
	v_mfma_f32_32x32x16_f16 v[18:33], v[66:69], v[34:37], v[18:33]
	v_min_u32_e32 v34, 0x78, v101
	v_mul_lo_u16_e32 v35, 0xbb, v34
	v_lshrrev_b16_e32 v35, 10, v35
	v_and_b32_e32 v35, 30, v35
	v_add_u32_e32 v105, v34, v35
	v_mad_u32_u24 v93, v105, s7, v42
	s_waitcnt lgkmcnt(0)
	v_mfma_f32_32x32x16_f16 v[2:17], v[66:69], v[38:41], v[2:17]
	v_add_u32_e32 v34, s8, v92
	v_add_u32_e32 v38, s8, v93
	ds_read_b128 v[34:37], v34
	ds_read_b128 v[38:41], v38
	v_add_u32_e32 v86, s9, v93
	s_waitcnt lgkmcnt(1)
	v_mfma_f32_32x32x16_f16 v[50:65], v[82:85], v[34:37], 0
	ds_read_b128 v[86:89], v86
	s_waitcnt lgkmcnt(1)
	v_mfma_f32_32x32x16_f16 v[34:49], v[82:85], v[38:41], 0
	v_add_u32_e32 v82, s9, v92
	ds_read_b128 v[82:85], v82
	s_waitcnt lgkmcnt(0)
	v_mfma_f32_32x32x16_f16 v[50:65], v[74:77], v[82:85], v[50:65]
	v_add_u32_e32 v82, s15, v93
	ds_read_b128 v[82:85], v82
	v_mfma_f32_32x32x16_f16 v[34:49], v[74:77], v[86:89], v[34:49]
	v_add_u32_e32 v74, s15, v92
	ds_read_b128 v[74:77], v74
	s_waitcnt lgkmcnt(0)
	v_mfma_f32_32x32x16_f16 v[50:65], v[78:81], v[74:77], v[50:65]
	v_add_u32_e32 v74, s16, v92
	ds_read_b128 v[74:77], v74
	v_mfma_f32_32x32x16_f16 v[34:49], v[78:81], v[82:85], v[34:49]
	v_add_u32_e32 v78, s16, v93
	ds_read_b128 v[78:81], v78
	s_waitcnt lgkmcnt(1)
	v_mfma_f32_32x32x16_f16 v[50:65], v[70:73], v[74:77], v[50:65]
	v_add_u32_e32 v74, s17, v93
	ds_read_b128 v[74:77], v74
	s_waitcnt lgkmcnt(1)
	v_mfma_f32_32x32x16_f16 v[34:49], v[70:73], v[78:81], v[34:49]
	v_add_u32_e32 v70, s17, v92
	ds_read_b128 v[70:73], v70
	s_waitcnt lgkmcnt(0)
	v_mfma_f32_32x32x16_f16 v[50:65], v[66:69], v[70:73], v[50:65]
	v_mfma_f32_32x32x16_f16 v[34:49], v[66:69], v[74:77], v[34:49]
	s_movk_i32 s7, 0x1cb0
	s_cselect_b32 s7, s7, 0x2a0
	v_add_u32_e32 v74, s7, v90
	ds_read_b128 v[74:77], v74
	v_add_u32_e32 v78, s7, v91
	ds_read_b128 v[78:81], v78
	s_movk_i32 s12, 0x1d30
	s_cselect_b32 s12, s12, 0xdd0
	s_movk_i32 s8, 0x1dc0
	s_cselect_b32 s8, s8, 0xe50
	s_movk_i32 s9, 0x1e40
	s_cselect_b32 s9, s9, 0xee0
	s_waitcnt vmcnt(0) lgkmcnt(1)
	v_mfma_f32_32x32x16_f16 v[18:33], v[108:111], v[74:77], v[18:33]
	v_add_u32_e32 v82, s12, v91
	ds_read_b128 v[82:85], v82
	s_waitcnt lgkmcnt(1)
	v_mfma_f32_32x32x16_f16 v[2:17], v[108:111], v[78:81], v[2:17]
	v_add_u32_e32 v78, s12, v90
	ds_read_b128 v[78:81], v78
	s_waitcnt lgkmcnt(0)
	v_mfma_f32_32x32x16_f16 v[18:33], v[118:121], v[78:81], v[18:33]
	v_add_u32_e32 v86, s8, v91
	ds_read_b128 v[86:89], v86
	v_mfma_f32_32x32x16_f16 v[2:17], v[118:121], v[82:85], v[2:17]
	v_add_u32_e32 v82, s8, v90
	ds_read_b128 v[82:85], v82
	s_waitcnt lgkmcnt(0)
	v_mfma_f32_32x32x16_f16 v[18:33], v[122:125], v[82:85], v[18:33]
	v_add_u32_e32 v82, s9, v90
	ds_read_b128 v[82:85], v82
	v_mfma_f32_32x32x16_f16 v[2:17], v[122:125], v[86:89], v[2:17]
	v_add_u32_e32 v86, s9, v91
	ds_read_b128 v[86:89], v86
	s_waitcnt lgkmcnt(1)
	v_mfma_f32_32x32x16_f16 v[18:33], v[94:97], v[82:85], v[18:33]
	s_waitcnt lgkmcnt(0)
	v_mfma_f32_32x32x16_f16 v[2:17], v[94:97], v[86:89], v[2:17]
	v_add_u32_e32 v82, s7, v92
	v_add_u32_e32 v86, s7, v93
	ds_read_b128 v[82:85], v82
	ds_read_b128 v[86:89], v86
	s_waitcnt lgkmcnt(1)
	v_mfma_f32_32x32x16_f16 v[50:65], v[108:111], v[82:85], v[50:65]
	v_add_u32_e32 v82, s12, v93
	ds_read_b128 v[82:85], v82
	s_waitcnt lgkmcnt(1)
	v_mfma_f32_32x32x16_f16 v[34:49], v[108:111], v[86:89], v[34:49]
	v_add_u32_e32 v66, s12, v92
	ds_read_b128 v[66:69], v66
	s_waitcnt lgkmcnt(0)
	v_mfma_f32_32x32x16_f16 v[50:65], v[118:121], v[66:69], v[50:65]
	v_add_u32_e32 v66, s8, v92
	ds_read_b128 v[66:69], v66
	v_mfma_f32_32x32x16_f16 v[34:49], v[118:121], v[82:85], v[34:49]
	v_add_u32_e32 v70, s8, v93
	ds_read_b128 v[70:73], v70
	s_waitcnt lgkmcnt(1)
	v_mfma_f32_32x32x16_f16 v[50:65], v[122:125], v[66:69], v[50:65]
	v_add_u32_e32 v66, s9, v92
	ds_read_b128 v[66:69], v66
	s_waitcnt lgkmcnt(1)
	v_mfma_f32_32x32x16_f16 v[34:49], v[122:125], v[70:73], v[34:49]
	v_add_u32_e32 v70, s9, v93
	ds_read_b128 v[70:73], v70
	s_waitcnt lgkmcnt(1)
	v_mfma_f32_32x32x16_f16 v[50:65], v[94:97], v[66:69], v[50:65]
	s_waitcnt lgkmcnt(0)
	v_mfma_f32_32x32x16_f16 v[34:49], v[94:97], v[70:73], v[34:49]
	s_cmpk_gt_u32 s3, 0x17f
	s_barrier
	s_cbranch_scc1 .LBB1_17
	s_mul_hi_u32 s7, s42, 0x55555556
	s_mul_i32 s7, s7, 3
	s_sub_i32 s7, s42, s7
	s_lshl_b32 s7, s7, 3
	s_add_i32 s8, s7, 0xb600
	s_cmpk_gt_u32 s3, 0xbf
	v_mad_u32_u24 v109, v115, 24, s7
	s_cselect_b32 s7, 0x60, 0
	v_or_b32_e32 v112, s7, v114
	v_mul_lo_u16_e32 v66, 0x4f, v112
	v_lshrrev_b16_e32 v66, 9, v66
	v_and_b32_e32 v66, 30, v66
	v_add_u32_e32 v66, v112, v66
	v_mov_b32_e32 v111, s8
	v_mul_u32_u24_e32 v110, 0x48, v115
	v_add_u32_e32 v107, 0xf550, v98
	v_mad_u32_u24 v113, v66, s6, v111
	ds_read_b128 v[76:79], v107 offset:5120
	v_add_u32_e32 v117, v113, v110
	ds_read2_b64 v[118:121], v117 offset0:4 offset1:5
	ds_read_b128 v[122:125], v98 offset:62800
	v_mul_u32_u24_e32 v108, 0x438, v115
	v_add_u32_e32 v113, v113, v108
	s_waitcnt lgkmcnt(2)
	v_mov_b32_e32 v66, v76
	v_mov_b32_e32 v67, v76
	v_mov_b32_e32 v68, v76
	v_mov_b32_e32 v69, v76
	v_mov_b32_e32 v70, v77
	v_mov_b32_e32 v71, v77
	v_mov_b32_e32 v72, v77
	v_mov_b32_e32 v73, v77
	v_mov_b32_e32 v74, v78
	v_mov_b32_e32 v75, v78
	v_mov_b32_e32 v76, v78
	v_mov_b32_e32 v77, v78
	v_mov_b32_e32 v78, v79
	v_mov_b32_e32 v80, v79
	v_mov_b32_e32 v81, v79
	s_movk_i32 s8, 0xd0
	v_mad_u32_u24 v112, v112, s8, v109
	s_waitcnt lgkmcnt(0)
	v_mfma_f32_32x32x16_f16 v[82:97], v[122:125], v[118:121], v[66:81]
	ds_read2_b64 v[118:121], v117 offset0:139 offset1:140
	ds_read_b128 v[122:125], v98 offset:63824
	s_waitcnt lgkmcnt(0)
	v_mfma_f32_32x32x16_f16 v[82:97], v[122:125], v[118:121], v[82:97]
	v_add_u32_e32 v118, 0x8d8, v117
	ds_read2_b64 v[118:121], v118 offset1:1
	ds_read_b128 v[122:125], v98 offset:64848
	s_waitcnt lgkmcnt(0)
	v_mfma_f32_32x32x16_f16 v[82:97], v[122:125], v[118:121], v[82:97]
	ds_read2_b64 v[118:121], v113 offset0:22 offset1:23
	ds_read_b128 v[122:125], v107 offset:3072
	v_add_u32_e32 v113, 0x890, v117
	s_waitcnt lgkmcnt(0)
	v_mfma_f32_32x32x16_f16 v[82:97], v[122:125], v[118:121], v[82:97]
	ds_read2_b64 v[118:121], v113 offset1:1
	ds_read_b128 v[122:125], v107 offset:4096
	s_waitcnt lgkmcnt(0)
	v_mfma_f32_32x32x16_f16 v[82:97], v[122:125], v[118:121], v[82:97]
	s_nop 11
	v_cvt_pk_f16_f32 v82, v82, v83
	v_cvt_pk_f16_f32 v83, v84, v85
	v_cvt_pk_f16_f32 v84, v86, v87
	v_cvt_pk_f16_f32 v85, v88, v89
	v_pk_max_f16 v82, v82, 0
	v_pk_max_f16 v83, v83, 0
	v_pk_max_f16 v84, v84, 0
	v_pk_max_f16 v85, v85, 0
	ds_write2_b64 v112, v[82:83], v[84:85] offset1:6
	v_cvt_pk_f16_f32 v82, v90, v91
	v_cvt_pk_f16_f32 v83, v92, v93
	v_cvt_pk_f16_f32 v84, v94, v95
	v_cvt_pk_f16_f32 v85, v96, v97
	v_pk_max_f16 v82, v82, 0
	v_pk_max_f16 v83, v83, 0
	v_pk_max_f16 v84, v84, 0
	v_pk_max_f16 v85, v85, 0
	ds_write2_b64 v112, v[82:83], v[84:85] offset0:12 offset1:18
	s_add_i32 s9, s7, 32
	v_or_b32_e32 v112, s9, v114
	v_mul_lo_u16_e32 v82, 0x4f, v112
	v_lshrrev_b16_e32 v82, 9, v82
	v_and_b32_e32 v82, 62, v82
	v_add_u32_e32 v82, v112, v82
	v_mad_u32_u24 v113, v82, s6, v111
	v_add_u32_e32 v117, v113, v110
	ds_read2_b64 v[118:121], v117 offset0:4 offset1:5
	ds_read_b128 v[122:125], v98 offset:62800
	v_add_u32_e32 v113, v113, v108
	v_mad_u32_u24 v112, v112, s8, v109
	s_waitcnt lgkmcnt(0)
	v_mfma_f32_32x32x16_f16 v[82:97], v[122:125], v[118:121], v[66:81]
	ds_read2_b64 v[118:121], v117 offset0:139 offset1:140
	ds_read_b128 v[122:125], v98 offset:63824
	s_waitcnt lgkmcnt(0)
	v_mfma_f32_32x32x16_f16 v[82:97], v[122:125], v[118:121], v[82:97]
	v_add_u32_e32 v118, 0x8d8, v117
	ds_read2_b64 v[118:121], v118 offset1:1
	ds_read_b128 v[122:125], v98 offset:64848
	s_waitcnt lgkmcnt(0)
	v_mfma_f32_32x32x16_f16 v[82:97], v[122:125], v[118:121], v[82:97]
	ds_read2_b64 v[118:121], v113 offset0:22 offset1:23
	ds_read_b128 v[122:125], v107 offset:3072
	v_add_u32_e32 v113, 0x890, v117
	s_waitcnt lgkmcnt(0)
	v_mfma_f32_32x32x16_f16 v[82:97], v[122:125], v[118:121], v[82:97]
	ds_read2_b64 v[118:121], v113 offset1:1
	ds_read_b128 v[122:125], v107 offset:4096
	s_waitcnt lgkmcnt(0)
	v_mfma_f32_32x32x16_f16 v[82:97], v[122:125], v[118:121], v[82:97]
	s_nop 11
	v_cvt_pk_f16_f32 v82, v82, v83
	v_cvt_pk_f16_f32 v83, v84, v85
	v_cvt_pk_f16_f32 v84, v86, v87
	v_cvt_pk_f16_f32 v85, v88, v89
	v_pk_max_f16 v82, v82, 0
	v_pk_max_f16 v83, v83, 0
	v_pk_max_f16 v84, v84, 0
	v_pk_max_f16 v85, v85, 0
	ds_write2_b64 v112, v[82:83], v[84:85] offset1:6
	v_cvt_pk_f16_f32 v82, v90, v91
	v_cvt_pk_f16_f32 v83, v92, v93
	v_cvt_pk_f16_f32 v84, v94, v95
	v_cvt_pk_f16_f32 v85, v96, v97
	v_pk_max_f16 v82, v82, 0
	v_pk_max_f16 v83, v83, 0
	v_pk_max_f16 v84, v84, 0
	v_pk_max_f16 v85, v85, 0
	ds_write2_b64 v112, v[82:83], v[84:85] offset0:12 offset1:18
	s_add_i32 s7, s7, 64
	v_or_b32_e32 v82, s7, v114
	v_min_u32_e32 v112, 0xa8, v82
	v_mul_lo_u16_e32 v82, 0x4f, v112
	v_lshrrev_b16_e32 v82, 9, v82
	v_and_b32_e32 v86, 62, v82
	ds_read_b128 v[82:85], v98 offset:62800
	v_add_u32_e32 v86, v112, v86
	v_mad_u32_u24 v111, v86, s6, v111
	v_add_u32_e32 v110, v111, v110
	ds_read2_b64 v[86:89], v110 offset0:4 offset1:5
	ds_read2_b64 v[90:93], v110 offset0:139 offset1:140
	v_add_u32_e32 v94, 0x890, v110
	ds_read2_b64 v[94:97], v94 offset1:1
	s_waitcnt lgkmcnt(2)
	v_mfma_f32_32x32x16_f16 v[66:81], v[82:85], v[86:89], v[66:81]
	ds_read_b128 v[82:85], v98 offset:63824
	ds_read_b128 v[86:89], v98 offset:64848
	s_waitcnt lgkmcnt(1)
	v_mfma_f32_32x32x16_f16 v[66:81], v[82:85], v[90:93], v[66:81]
	v_add_u32_e32 v82, 0x8d8, v110
	ds_read2_b64 v[82:85], v82 offset1:1
	v_add_u32_e32 v90, v111, v108
	ds_read2_b64 v[90:93], v90 offset0:22 offset1:23
	s_waitcnt lgkmcnt(1)
	v_mfma_f32_32x32x16_f16 v[66:81], v[86:89], v[82:85], v[66:81]
	ds_read_b128 v[82:85], v107 offset:3072
	ds_read_b128 v[86:89], v107 offset:4096
	s_waitcnt lgkmcnt(1)
	v_mfma_f32_32x32x16_f16 v[66:81], v[82:85], v[90:93], v[66:81]
	v_mad_u32_u24 v82, v112, s8, v109
	s_waitcnt lgkmcnt(0)
	v_mfma_f32_32x32x16_f16 v[66:81], v[86:89], v[94:97], v[66:81]
	s_nop 11
	v_cvt_pk_f16_f32 v66, v66, v67
	v_cvt_pk_f16_f32 v67, v68, v69
	v_cvt_pk_f16_f32 v68, v70, v71
	v_cvt_pk_f16_f32 v69, v72, v73
	v_cvt_pk_f16_f32 v70, v74, v75
	v_cvt_pk_f16_f32 v71, v76, v77
	v_cvt_pk_f16_f32 v72, v78, v79
	v_cvt_pk_f16_f32 v73, v80, v81
	v_pk_max_f16 v66, v66, 0
	v_pk_max_f16 v67, v67, 0
	v_pk_max_f16 v68, v68, 0
	v_pk_max_f16 v69, v69, 0
	v_pk_max_f16 v70, v70, 0
	v_pk_max_f16 v71, v71, 0
	v_pk_max_f16 v72, v72, 0
	v_pk_max_f16 v73, v73, 0
	ds_write2_b64 v82, v[66:67], v[68:69] offset1:6
	ds_write2_b64 v82, v[70:71], v[72:73] offset0:12 offset1:18
.LBB1_17:
	s_mul_i32 s16, s66, 15
	s_lshl_b32 s14, s67, 3
	s_addk_i32 s16, 0x48
	s_add_i32 s6, s16, s14
	s_lshl_b32 s6, s6, 6
	v_or_b32_e32 v66, s6, v100
	v_mov_b32_e32 v67, 0
	v_lshl_add_u64 v[68:69], v[66:67], 4, s[22:23]
	global_load_dwordx4 v[70:73], v[68:69], off
	s_add_i32 s7, s6, 64
	v_or_b32_e32 v66, s7, v100
	v_lshl_add_u64 v[68:69], v[66:67], 4, s[22:23]
	global_load_dwordx4 v[74:77], v[68:69], off
	s_add_i32 s7, s6, 0x80
	v_or_b32_e32 v66, s7, v100
	v_lshl_add_u64 v[68:69], v[66:67], 4, s[22:23]
	global_load_dwordx4 v[78:81], v[68:69], off
	s_addk_i32 s6, 0xc0
	v_or_b32_e32 v66, s6, v100
	v_lshl_add_u64 v[68:69], v[66:67], 4, s[22:23]
	global_load_dwordx4 v[82:85], v[68:69], off
	s_add_i32 s7, s6, 64
	v_or_b32_e32 v66, s7, v100
	v_lshl_add_u64 v[68:69], v[66:67], 4, s[22:23]
	global_load_dwordx4 v[108:111], v[68:69], off
	s_add_i32 s7, s6, 0x80
	v_or_b32_e32 v66, s7, v100
	v_lshl_add_u64 v[68:69], v[66:67], 4, s[22:23]
	global_load_dwordx4 v[118:121], v[68:69], off
	s_add_i32 s7, s6, 0xc0
	v_or_b32_e32 v66, s7, v100
	v_lshl_add_u64 v[68:69], v[66:67], 4, s[22:23]
	global_load_dwordx4 v[122:125], v[68:69], off
	s_and_b64 s[74:75], vcc, exec
	s_movk_i32 s7, 0x100
	s_cselect_b32 s7, 0xc0, s7
	s_add_i32 s7, s6, s7
	v_or_b32_e32 v66, s7, v100
	v_lshl_add_u64 v[112:113], v[66:67], 4, s[22:23]
	s_mul_i32 s66, s66, 48
	v_mul_u32_u24_e32 v69, 0xd0, v115
	v_mul_u32_u24_e32 v66, 0xd0, v103
	v_mul_u32_u24_e32 v86, 0xd0, v106
	s_movk_i32 s8, 0x9c0
	v_add3_u32 v68, v66, s66, v69
	v_add3_u32 v66, v86, s66, v69
	v_mad_u32_u24 v94, v115, s8, v68
	s_and_b64 s[6:7], vcc, exec
	v_mad_u32_u24 v96, v115, s8, v66
	v_cndmask_b32_e32 v95, v68, v94, vcc
	s_cselect_b32 s6, 0x1b0, 0
	v_cndmask_b32_e32 v97, v66, v96, vcc
	v_add_u32_e32 v86, s6, v95
	v_add_u32_e32 v90, s6, v97
	s_waitcnt lgkmcnt(0)
	s_barrier
	ds_read_b128 v[86:89], v86
	ds_read_b128 v[90:93], v90
	s_movk_i32 s7, 0x1530
	s_cselect_b32 s7, s7, 0xa90
	s_cselect_b32 s9, 32, 0x15f0
	s_movk_i32 s12, 0xab0
	s_cselect_b32 s12, s12, 0x1a0
	s_waitcnt vmcnt(6) lgkmcnt(1)
	v_mfma_f32_32x32x16_f16 v[18:33], v[70:73], v[86:89], v[18:33]
	v_add_u32_e32 v86, s7, v68
	ds_read_b128 v[86:89], v86
	s_waitcnt lgkmcnt(1)
	v_mfma_f32_32x32x16_f16 v[2:17], v[70:73], v[90:93], v[2:17]
	v_add_u32_e32 v90, s7, v66
	ds_read_b128 v[90:93], v90
	s_waitcnt vmcnt(5) lgkmcnt(1)
	v_mfma_f32_32x32x16_f16 v[18:33], v[74:77], v[86:89], v[18:33]
	v_add_u32_e32 v86, s9, v68
	ds_read_b128 v[86:89], v86
	s_waitcnt lgkmcnt(1)
	v_mfma_f32_32x32x16_f16 v[2:17], v[74:77], v[90:93], v[2:17]
	v_add_u32_e32 v90, s9, v66
	ds_read_b128 v[90:93], v90
	s_waitcnt vmcnt(4) lgkmcnt(1)
	v_mfma_f32_32x32x16_f16 v[18:33], v[78:81], v[86:89], v[18:33]
	v_cndmask_b32_e32 v86, v94, v68, vcc
	v_add_u32_e32 v86, s12, v86
	ds_read_b128 v[86:89], v86
	s_waitcnt lgkmcnt(1)
	v_mfma_f32_32x32x16_f16 v[2:17], v[78:81], v[90:93], v[2:17]
	v_cndmask_b32_e32 v90, v96, v66, vcc
	v_add_u32_e32 v90, s12, v90
	ds_read_b128 v[90:93], v90
	s_waitcnt vmcnt(3) lgkmcnt(1)
	v_mfma_f32_32x32x16_f16 v[18:33], v[82:85], v[86:89], v[18:33]
	v_mul_u32_u24_e32 v86, 0xd0, v104
	v_mul_u32_u24_e32 v87, 0xd0, v105
	v_add3_u32 v94, v86, s66, v69
	v_add3_u32 v69, v87, s66, v69
	v_mad_u32_u24 v96, v115, s8, v94
	v_mad_u32_u24 v103, v115, s8, v69
	s_waitcnt lgkmcnt(0)
	v_mfma_f32_32x32x16_f16 v[2:17], v[82:85], v[90:93], v[2:17]
	v_cndmask_b32_e32 v104, v94, v96, vcc
	v_cndmask_b32_e32 v105, v69, v103, vcc
	v_add_u32_e32 v86, s6, v104
	v_add_u32_e32 v90, s6, v105
	ds_read_b128 v[86:89], v86
	ds_read_b128 v[90:93], v90
	s_waitcnt lgkmcnt(1)
	v_mfma_f32_32x32x16_f16 v[50:65], v[70:73], v[86:89], v[50:65]
	v_add_u32_e32 v86, s7, v69
	ds_read_b128 v[86:89], v86
	s_waitcnt lgkmcnt(1)
	v_mfma_f32_32x32x16_f16 v[34:49], v[70:73], v[90:93], v[34:49]
	v_add_u32_e32 v70, s7, v94
	ds_read_b128 v[70:73], v70
	s_waitcnt lgkmcnt(0)
	v_mfma_f32_32x32x16_f16 v[50:65], v[74:77], v[70:73], v[50:65]
	v_add_u32_e32 v70, s9, v94
	ds_read_b128 v[70:73], v70
	v_mfma_f32_32x32x16_f16 v[34:49], v[74:77], v[86:89], v[34:49]
	global_load_dwordx4 v[86:89], v[112:113], off
	v_add_u32_e32 v74, s9, v69
	ds_read_b128 v[74:77], v74
	s_waitcnt lgkmcnt(1)
	v_mfma_f32_32x32x16_f16 v[50:65], v[78:81], v[70:73], v[50:65]
	v_cndmask_b32_e32 v70, v96, v94, vcc
	v_add_u32_e32 v70, s12, v70
	ds_read_b128 v[70:73], v70
	s_waitcnt lgkmcnt(1)
	v_mfma_f32_32x32x16_f16 v[34:49], v[78:81], v[74:77], v[34:49]
	v_cndmask_b32_e32 v74, v103, v69, vcc
	v_add_u32_e32 v74, s12, v74
	ds_read_b128 v[74:77], v74
	s_waitcnt lgkmcnt(1)
	v_mfma_f32_32x32x16_f16 v[50:65], v[82:85], v[70:73], v[50:65]
	s_waitcnt lgkmcnt(0)
	v_mfma_f32_32x32x16_f16 v[34:49], v[82:85], v[74:77], v[34:49]
	s_movk_i32 s24, 0x1610
	s_and_b64 s[16:17], vcc, exec
	s_cselect_b32 s16, s24, 0x1520
	v_add_u32_e32 v78, s16, v68
	ds_read_b128 v[78:81], v78
	v_add_u32_e32 v82, s16, v66
	ds_read_b128 v[82:85], v82
	s_cselect_b32 s6, 0x1c0, 16
	s_movk_i32 s7, 0x1540
	s_cselect_b32 s7, s7, 0xaa0
	s_movk_i32 s8, 0x1600
	s_cselect_b32 s8, 0x1540, s8
	s_waitcnt vmcnt(3) lgkmcnt(1)
	v_mfma_f32_32x32x16_f16 v[18:33], v[108:111], v[78:81], v[18:33]
	v_add_u32_e32 v70, s6, v95
	ds_read_b128 v[70:73], v70
	s_waitcnt lgkmcnt(1)
	v_mfma_f32_32x32x16_f16 v[2:17], v[108:111], v[82:85], v[2:17]
	v_add_u32_e32 v82, s6, v97
	ds_read_b128 v[82:85], v82
	s_waitcnt vmcnt(2) lgkmcnt(1)
	v_mfma_f32_32x32x16_f16 v[18:33], v[118:121], v[70:73], v[18:33]
	v_add_u32_e32 v90, s7, v68
	ds_read_b128 v[90:93], v90
	v_add_u32_e32 v68, s8, v68
	s_waitcnt lgkmcnt(1)
	v_mfma_f32_32x32x16_f16 v[2:17], v[118:121], v[82:85], v[2:17]
	v_add_u32_e32 v82, s7, v66
	ds_read_b128 v[82:85], v82
	v_add_u32_e32 v66, s8, v66
	s_waitcnt vmcnt(0) lgkmcnt(1)
	v_mfma_f32_32x32x16_f16 v[18:33], v[122:125], v[90:93], v[18:33]
	ds_read_b128 v[90:93], v68
	v_cndmask_b32_e64 v86, v86, 0, vcc
	v_cndmask_b32_e64 v87, v87, 0, vcc
	v_cndmask_b32_e64 v88, v88, 0, vcc
	v_cndmask_b32_e64 v89, v89, 0, vcc
	s_waitcnt lgkmcnt(1)
	v_mfma_f32_32x32x16_f16 v[2:17], v[122:125], v[82:85], v[2:17]
	ds_read_b128 v[82:85], v66
	s_waitcnt lgkmcnt(1)
	v_mfma_f32_32x32x16_f16 v[18:33], v[86:89], v[90:93], v[18:33]
	s_waitcnt lgkmcnt(0)
	v_mfma_f32_32x32x16_f16 v[2:17], v[86:89], v[82:85], v[2:17]
	v_add_u32_e32 v70, s16, v94
	v_add_u32_e32 v74, s16, v69
	ds_read_b128 v[70:73], v70
	ds_read_b128 v[74:77], v74
	s_waitcnt lgkmcnt(1)
	v_mfma_f32_32x32x16_f16 v[50:65], v[108:111], v[70:73], v[50:65]
	v_add_u32_e32 v70, s6, v104
	ds_read_b128 v[70:73], v70
	s_waitcnt lgkmcnt(1)
	v_mfma_f32_32x32x16_f16 v[34:49], v[108:111], v[74:77], v[34:49]
	v_add_u32_e32 v74, s6, v105
	ds_read_b128 v[74:77], v74
	s_waitcnt lgkmcnt(1)
	v_mfma_f32_32x32x16_f16 v[50:65], v[118:121], v[70:73], v[50:65]
	v_add_u32_e32 v70, s7, v94
	ds_read_b128 v[70:73], v70
	s_waitcnt lgkmcnt(1)
	v_mfma_f32_32x32x16_f16 v[34:49], v[118:121], v[74:77], v[34:49]
	v_add_u32_e32 v74, s7, v69
	ds_read_b128 v[74:77], v74
	s_waitcnt lgkmcnt(1)
	v_mfma_f32_32x32x16_f16 v[50:65], v[122:125], v[70:73], v[50:65]
	v_add_u32_e32 v70, s8, v94
	ds_read_b128 v[70:73], v70
	s_waitcnt lgkmcnt(1)
	v_mfma_f32_32x32x16_f16 v[34:49], v[122:125], v[74:77], v[34:49]
	v_add_u32_e32 v74, s8, v69
	ds_read_b128 v[74:77], v74
	s_waitcnt lgkmcnt(1)
	v_mfma_f32_32x32x16_f16 v[50:65], v[86:89], v[70:73], v[50:65]
	s_waitcnt lgkmcnt(0)
	v_mfma_f32_32x32x16_f16 v[34:49], v[86:89], v[74:77], v[34:49]
	s_cmpk_lt_i32 s2, 0x200
	s_movk_i32 s8, 0xd3
	s_cselect_b64 s[6:7], -1, 0
	v_cmp_gt_u32_e32 vcc, s8, v0
	s_and_b64 s[8:9], s[6:7], vcc
	s_barrier
	s_and_saveexec_b64 s[6:7], s[8:9]
	s_cbranch_execz .LBB1_19
	s_add_i32 s8, s2, 0x200
	s_mul_hi_i32 s9, s8, 0x6978
	s_mulk_i32 s8, 0x6978
	s_add_u32 s8, s20, s8
	s_addc_u32 s9, s21, s9
	v_lshlrev_b32_e32 v14, 7, v0
	global_load_dword v67, v14, s[8:9]

.LBB1_21:
	s_or_b64 exec, exec, s[6:7]
	s_cmpk_lt_u32 s3, 0x180
	s_cbranch_scc0 .Lmy_p6prep
	s_mov_b64 s[8:9], 0
	s_branch .LBB1_41
.Lmy_p6prep:
	v_and_b32_e32 v6, 0x7f, v0
	v_cmp_gt_u32_e64 s[6:7], s8, v6
	s_movk_i32 s8, 0x78
	v_cmp_lt_u32_e32 vcc, s8, v6
	s_and_saveexec_b64 s[8:9], vcc
	s_xor_b64 s[8:9], exec, s[8:9]
	s_movk_i32 s12, 0x79
	v_cmp_ne_u32_e32 vcc, s12, v6
	s_nop 1
	v_cndmask_b32_e32 v66, 0, v6, vcc
	s_or_saveexec_b64 s[12:13], s[8:9]
	v_mov_b32_e32 v49, 0
	v_mov_b32_e32 v48, 0
	s_xor_b64 exec, exec, s[12:13]
	s_cbranch_execz .LBB1_39
	v_mul_lo_u16_e32 v2, 0xbb, v6
	v_lshrrev_b16_e32 v5, 11, v2
	s_movk_i32 s8, 0x41
	v_mad_i32_i24 v3, v5, -11, v6
	v_add_u32_e32 v2, -5, v5
	v_sub_u32_e32 v4, 5, v5
	v_cmp_lt_u32_e32 vcc, s8, v6
	v_sub_u32_e32 v7, 5, v3
	v_mov_b32_e32 v66, 1
	v_cndmask_b32_e32 v2, v4, v2, vcc
	v_add_u32_e32 v4, -5, v3
	v_cmp_lt_i32_e32 vcc, 5, v3
	s_nop 1
	v_cndmask_b32_e32 v4, v7, v4, vcc
	v_max_i32_e32 v2, v2, v4
	v_cmp_ne_u32_e32 vcc, 0, v2
	s_and_saveexec_b64 s[14:15], vcc
	s_cbranch_execz .LBB1_38
	v_sub_u32_e32 v7, 5, v2
	v_cmp_ne_u32_e32 vcc, v7, v5
	v_cmp_le_i32_e64 s[8:9], v3, v7
	s_or_b64 s[8:9], vcc, s[8:9]
	s_and_saveexec_b64 s[16:17], s[8:9]
	s_xor_b64 s[16:17], exec, s[16:17]
	s_cbranch_execz .LBB1_35
	v_add_u32_e32 v8, 5, v2
	v_cmp_ne_u32_e32 vcc, v3, v8
	v_cmp_ge_i32_e64 s[8:9], v7, v5
	s_or_b64 s[8:9], vcc, s[8:9]
	s_and_saveexec_b64 s[18:19], s[8:9]
	s_xor_b64 s[18:19], exec, s[18:19]
	s_cbranch_execz .LBB1_32
	v_cmp_ne_u32_e32 vcc, v8, v5
	v_cmp_ge_i32_e64 s[8:9], v3, v8
	v_add_u32_e32 v7, -5, v2
	s_or_b64 s[8:9], vcc, s[8:9]
	s_and_saveexec_b64 s[20:21], s[8:9]
	s_xor_b64 s[8:9], exec, s[20:21]
	v_mul_lo_u32 v3, v2, 6
	v_add3_u32 v4, v3, v5, v7
	s_andn2_saveexec_b64 s[8:9], s[8:9]
	v_lshlrev_b32_e32 v4, 2, v2
	v_add3_u32 v4, v4, v3, v7
	s_or_b64 exec, exec, s[8:9]

.LBB1_39:
	s_or_b64 exec, exec, s[12:13]
	s_cmpk_gt_u32 s3, 0x17f
	s_cselect_b64 s[8:9], -1, 0
	s_cmpk_lt_u32 s3, 0x180
	v_mov_b32_e32 v76, 0
	v_mov_b32_e32 v77, 0
	v_mov_b32_e32 v70, 0
	v_mov_b32_e32 v71, 0
	v_mov_b32_e32 v68, 0
	v_mov_b32_e32 v69, 0
	v_mov_b32_e32 v64, 0
	v_mov_b32_e32 v65, 0
	v_mov_b32_e32 v62, 0
	v_mov_b32_e32 v63, 0
	v_mov_b32_e32 v60, 0
	v_mov_b32_e32 v61, 0
	v_mov_b32_e32 v58, 0
	v_mov_b32_e32 v59, 0
	v_mov_b32_e32 v56, 0
	v_mov_b32_e32 v57, 0
	v_mov_b32_e32 v54, 0
	v_mov_b32_e32 v55, 0
	v_mov_b32_e32 v52, 0
	v_mov_b32_e32 v53, 0
	s_cbranch_scc1 .LBB1_41
	v_min_i32_e32 v2, 0x79, v66
	v_mul_lo_u32 v2, v2, 21
	v_ashrrev_i32_e32 v3, 31, v2
	v_lshl_add_u64 v[24:25], v[2:3], 2, s[26:27]
	global_load_dwordx4 v[2:5], v[24:25], off
	global_load_dwordx4 v[8:11], v[24:25], off offset:16
	global_load_dwordx4 v[12:15], v[24:25], off offset:32
	global_load_dwordx4 v[16:19], v[24:25], off offset:48
	global_load_dwordx4 v[20:23], v[24:25], off offset:64
	global_load_dword v49, v[24:25], off offset:80
	s_load_dwordx16 s[12:27], s[28:29], 0x0
	s_load_dword s56, s[28:29], 0x50
	s_load_dwordx4 s[52:55], s[28:29], 0x40
	s_movk_i32 s43, 0x79
	v_cmp_eq_u32_e32 vcc, s43, v6
	s_nop 1
	v_cndmask_b32_e64 v24, 0, 1.0, vcc
	s_waitcnt vmcnt(5) lgkmcnt(0)
	v_pk_fma_f32 v[76:77], v[24:25], s[12:13], v[2:3] op_sel_hi:[0,1,1]
	v_pk_fma_f32 v[70:71], v[24:25], s[14:15], v[4:5] op_sel_hi:[0,1,1]
	s_waitcnt vmcnt(4)
	v_pk_fma_f32 v[68:69], v[24:25], s[16:17], v[8:9] op_sel_hi:[0,1,1]
	v_pk_fma_f32 v[64:65], v[24:25], s[18:19], v[10:11] op_sel_hi:[0,1,1]
	s_waitcnt vmcnt(3)
	v_pk_fma_f32 v[62:63], v[24:25], s[20:21], v[12:13] op_sel_hi:[0,1,1]
	v_pk_fma_f32 v[60:61], v[24:25], s[22:23], v[14:15] op_sel_hi:[0,1,1]
	s_waitcnt vmcnt(2)
	v_pk_fma_f32 v[58:59], v[24:25], s[24:25], v[16:17] op_sel_hi:[0,1,1]
	v_pk_fma_f32 v[56:57], v[24:25], s[26:27], v[18:19] op_sel_hi:[0,1,1]
	s_waitcnt vmcnt(1)
	v_pk_fma_f32 v[54:55], v[24:25], s[52:53], v[20:21] op_sel_hi:[0,1,1]
	v_pk_fma_f32 v[52:53], v[24:25], s[54:55], v[22:23] op_sel_hi:[0,1,1]
	s_waitcnt vmcnt(0)
	v_fmac_f32_e32 v49, s56, v24
